# attention row-max chain: NaN-canonicalising self-max ops removed (three ops become one at two places per tile); conversion remap and loop reschedule kept
# speedup vs baseline: 1.0085x; 1.0014x over previous
; __device__ __forceinline__ void partialSM(f32x16& p0, f32x16& p1, float& m_reg, float& alpha, const bool first) {
;     float ma = max3f(p0[0], p0[1], p0[2]), mb = max3f(p0[3], p0[4], p0[5]), mc = max3f(p0[6], p0[7], p0[8]), md = max3f(p0[9], p0[10], p0[11]);
;     ma = max3f(ma, p0[12], p0[13]); mb = max3f(mb, p0[14], p0[15]); mc = max3f(mc, p1[0], p1[1]); md = max3f(md, p1[2], p1[3]);
;     ma = max3f(ma, p1[4], p1[5]); mb = max3f(mb, p1[6], p1[7]); mc = max3f(mc, p1[8], p1[9]); md = max3f(md, p1[10], p1[11]);
;     ma = max3f(ma, p1[12], p1[13]); mb = max3f(mb, p1[14], p1[15]);
;     float pmax = fmaxf(max3f(ma, mb, mc), md);
;     { auto rr = __builtin_amdgcn_permlane32_swap(__float_as_uint(pmax), __float_as_uint(pmax), false, false);
;       pmax = fmaxf(__uint_as_float(rr[0]), __uint_as_float(rr[1])); }
;     const float u = pmax - PSH;
;     if (__builtin_expect(!first && __all(u <= THR2), 1)) { alpha = 1.f; }
;     else { const float dl = first ? u : fmaxf(u, 0.f); alpha = __builtin_amdgcn_exp2f(-dl); m_reg += dl;
; #pragma unroll
;         for (int r = 0; r < 16; ++r) { p0[r] -= dl; p1[r] -= dl; } }
; #pragma unroll
;     for (int r = 0; r < 16; ++r) p0[r] = __builtin_amdgcn_exp2f(p0[r]);
; }
; __device__ __forceinline__ void finishSM(f32x16& p0, f32x16& p1, float alpha, float& l_reg, v8i& pa) {
; #pragma unroll
;     for (int r = 0; r < 16; ++r) p1[r] = __builtin_amdgcn_exp2f(p1[r]);
;     float sa = p0[0] + p0[1], sb = p0[2] + p0[3], sc = p0[4] + p0[5], sd = p0[6] + p0[7];
;     sa += p0[8]; sb += p0[9]; sc += p0[10]; sd += p0[11]; sa += p0[12]; sb += p0[13]; sc += p0[14]; sd += p0[15];
; #pragma unroll
;     for (int r = 0; r < 16; r += 4) { sa += p1[r]; sb += p1[r + 1]; sc += p1[r + 2]; sd += p1[r + 3]; }
;     float ps = (sa + sb) + (sc + sd);
;     { auto rr = __builtin_amdgcn_permlane32_swap(__float_as_uint(ps), __float_as_uint(ps), false, false);
;       ps = __uint_as_float(rr[0]) + __uint_as_float(rr[1]); }
;     l_reg = l_reg * alpha + ps;
; #pragma unroll
;     for (int c = 0; c < 4; ++c) { pa[c] = (int)pk4_fp8(p0[4 * c], p0[4 * c + 1], p0[4 * c + 2], p0[4 * c + 3]);
;         pa[4 + c] = (int)pk4_fp8(p1[4 * c], p1[4 * c + 1], p1[4 * c + 2], p1[4 * c + 3]); }
; }
; __device__ __forceinline__ void qkt(f32x16& p0, f32x16& p1, const float m_reg, const char* Ks, const v8i* q8, int r32, int hi) {
;     { const float ini = PSH - m_reg;
.LBB0_553:
	v_sub_f32_e32 v80, 0x40400000, v180
	v_mov_b32_e32 v81, v80
	v_mov_b32_e32 v82, v80
	v_mov_b32_e32 v83, v80
	v_mov_b32_e32 v84, v80
	v_mov_b32_e32 v85, v80
	v_mov_b32_e32 v86, v80
	v_mov_b32_e32 v87, v80
	v_mov_b32_e32 v88, v80
	v_mov_b32_e32 v89, v80
	v_mov_b32_e32 v90, v80
	v_mov_b32_e32 v91, v80
	v_mov_b32_e32 v92, v80
	v_mov_b32_e32 v93, v80
	v_mov_b32_e32 v94, v80
	v_mov_b32_e32 v95, v80
	v_exp_f32_e32 v228, v64
	v_exp_f32_e32 v230, v65
	s_waitcnt lgkmcnt(0)
	v_mfma_scale_f32_32x32x64_f8f6f4 v[96:111], v[96:103], v[120:127], v[80:95], v201, v200 op_sel_hi:[0,0,0]
	v_exp_f32_e32 v222, v66
	v_exp_f32_e32 v223, v67
	v_exp_f32_e32 v229, v68
	v_exp_f32_e32 v231, v69
	v_exp_f32_e32 v226, v70
	v_exp_f32_e32 v227, v71
	v_add_f32_e32 v64, v215, v216
	v_add_f32_e32 v65, v190, v192
	v_add_f32_e32 v66, v213, v214
	v_add_f32_e32 v67, v195, v212
	v_exp_f32_e32 v224, v72
	v_exp_f32_e32 v225, v73
	v_exp_f32_e32 v184, v74
	v_exp_f32_e32 v217, v75
	v_add_f32_e32 v64, v194, v64
	v_mfma_scale_f32_32x32x64_f8f6f4 v[80:95], v[136:143], v[120:127], v[80:95], v201, v200 op_sel_hi:[0,0,0]
	ds_read_b128 v[136:139], v164 offset:64
	ds_read_b128 v[140:143], v164 offset:80
	ds_read_b128 v[144:147], v164 offset:6720
	ds_read_b128 v[148:151], v164 offset:6736
	v_add_f32_e32 v65, v211, v65
	v_add_f32_e32 v66, v186, v66
	v_add_f32_e32 v67, v187, v67
	v_exp_f32_e32 v220, v76
	v_exp_f32_e32 v221, v77
	v_exp_f32_e32 v218, v78
	v_exp_f32_e32 v219, v79
	v_add_f32_e32 v64, v191, v64
	v_add_f32_e32 v65, v193, v65
	v_add_f32_e32 v66, v188, v66
	v_add_f32_e32 v67, v189, v67
	v_add_f32_e32 v64, v228, v64
	v_add_f32_e32 v65, v230, v65
	v_add_f32_e32 v66, v222, v66
	s_waitcnt lgkmcnt(0)
	v_mfma_scale_f32_32x32x64_f8f6f4 v[96:111], v[136:143], v[128:135], v[96:111], v201, v200 op_sel_hi:[0,0,0]
	v_add_f32_e32 v67, v223, v67
	v_add_f32_e32 v64, v229, v64
	v_add_f32_e32 v65, v231, v65
	v_add_f32_e32 v66, v226, v66
	v_add_f32_e32 v67, v227, v67
	v_add_f32_e32 v64, v224, v64
	v_add_f32_e32 v65, v225, v65
	v_add_f32_e32 v66, v184, v66
	v_add_f32_e32 v67, v217, v67
	v_add_f32_e32 v64, v220, v64
	v_add_f32_e32 v65, v221, v65
	v_add_f32_e32 v66, v218, v66
	v_add_f32_e32 v67, v219, v67
	v_add_f32_e32 v64, v65, v64
	v_add_f32_e32 v65, v66, v67
	v_mfma_scale_f32_32x32x64_f8f6f4 v[80:95], v[144:151], v[128:135], v[80:95], v201, v200 op_sel_hi:[0,0,0]
	ds_read_b128 v[136:139], v164 offset:128
	ds_read_b128 v[140:143], v164 offset:144
	ds_read_b128 v[144:147], v164 offset:6784
	ds_read_b128 v[148:151], v164 offset:6800
	v_add_f32_e32 v182, v65, v64
	v_mov_b32_e32 v183, v182
	v_cvt_pk_fp8_f32 v232, v215, v216
	v_cvt_pk_fp8_f32 v236, v228, v230
	v_cvt_pk_fp8_f32 v233, v213, v214
	v_cvt_pk_fp8_f32 v237, v229, v231
	v_cvt_pk_fp8_f32 v234, v194, v211
	v_cvt_pk_fp8_f32 v238, v224, v225
	v_cvt_pk_fp8_f32 v235, v191, v193
	v_cvt_pk_fp8_f32 v239, v220, v221
	v_permlane32_swap_b32_e32 v182, v183
	s_waitcnt lgkmcnt(0)
	v_mfma_scale_f32_32x32x64_f8f6f4 v[96:111], v[136:143], v[112:119], v[96:111], v201, v200 op_sel_hi:[0,0,0]
	v_cvt_pk_fp8_f32 v232, v190, v192 op_sel:[0,0,1]
	v_cvt_pk_fp8_f32 v236, v222, v223 op_sel:[0,0,1]
	v_cvt_pk_fp8_f32 v233, v195, v212 op_sel:[0,0,1]
	v_cvt_pk_fp8_f32 v237, v226, v227 op_sel:[0,0,1]
	v_cvt_pk_fp8_f32 v234, v186, v187 op_sel:[0,0,1]
	v_cvt_pk_fp8_f32 v238, v184, v217 op_sel:[0,0,1]
	v_cvt_pk_fp8_f32 v235, v188, v189 op_sel:[0,0,1]
	v_cvt_pk_fp8_f32 v239, v218, v219 op_sel:[0,0,1]
	v_mfma_scale_f32_32x32x64_f8f6f4 v[80:95], v[144:151], v[112:119], v[80:95], v201, v200 op_sel_hi:[0,0,0]
	s_mul_i32 s15, s10, 0x5c00
	s_add_i32 s11, s15, 0
	v_add_u32_e32 v64, s11, v161
	v_add_u32_e32 v176, v64, v179
	ds_read_b128 v[144:147], v176 offset:13312
	ds_read_b128 v[148:151], v176 offset:13328
	ds_read_b128 v[136:139], v176 offset:15872
	ds_read_b128 v[140:143], v176 offset:15888
	ds_read_b128 v[72:75], v176 offset:18432
	ds_read_b128 v[76:79], v176 offset:18448
	ds_read_b128 v[64:67], v176 offset:20992
	ds_read_b128 v[68:71], v176 offset:21008
	v_max_f32_e32 v164, v96, v97
	v_max3_f32 v165, v99, v100, v101
	v_max3_f32 v164, v164, v98, v108
	v_max3_f32 v165, v165, v110, v111
	v_max3_f32 v166, v102, v103, v104
	v_max3_f32 v167, v105, v106, v107
	s_waitcnt lgkmcnt(0)
	v_mfma_scale_f32_32x32x64_f8f6f4 v[0:15], v[232:239], v[144:151], v[0:15], v201, v201 op_sel_hi:[0,0,0]
	v_max3_f32 v164, v164, v109, v84
	v_max3_f32 v165, v165, v86, v87
	v_max3_f32 v166, v166, v80, v81
	v_max3_f32 v167, v167, v82, v83
	v_max3_f32 v164, v164, v85, v92
	v_max3_f32 v165, v165, v94, v95
	v_max3_f32 v166, v166, v88, v89
	v_max3_f32 v167, v167, v90, v91
	v_mfma_scale_f32_32x32x64_f8f6f4 v[48:63], v[232:239], v[136:143], v[48:63], v201, v201 op_sel_hi:[0,0,0]
	v_max3_f32 v164, v164, v93, v165
	v_max3_f32 v164, v164, v166, v167
	v_mov_b32_e32 v165, v164
	s_nop 1
	v_permlane32_swap_b32_e32 v164, v165
	v_max_f32_e32 v164, v164, v165
	v_add_f32_e32 v165, 0xc0400000, v164
	s_mov_b32 s0, 0x40b8aa3b
	v_cmp_ge_f32_e32 vcc, s0, v165
	s_cmp_eq_u64 vcc, exec
	v_mov_b32_e32 v185, 1.0
	s_cbranch_scc0 .LBB0_570

; __device__ __forceinline__ void partialSM(f32x16& p0, f32x16& p1, float& m_reg, float& alpha, const bool first) {
;     float ma = max3f(p0[0], p0[1], p0[2]), mb = max3f(p0[3], p0[4], p0[5]), mc = max3f(p0[6], p0[7], p0[8]), md = max3f(p0[9], p0[10], p0[11]);
;     ma = max3f(ma, p0[12], p0[13]); mb = max3f(mb, p0[14], p0[15]); mc = max3f(mc, p1[0], p1[1]); md = max3f(md, p1[2], p1[3]);
;     ma = max3f(ma, p1[4], p1[5]); mb = max3f(mb, p1[6], p1[7]); mc = max3f(mc, p1[8], p1[9]); md = max3f(md, p1[10], p1[11]);
;     ma = max3f(ma, p1[12], p1[13]); mb = max3f(mb, p1[14], p1[15]);
;     float pmax = fmaxf(max3f(ma, mb, mc), md);
;     { auto rr = __builtin_amdgcn_permlane32_swap(__float_as_uint(pmax), __float_as_uint(pmax), false, false);
;       pmax = fmaxf(__uint_as_float(rr[0]), __uint_as_float(rr[1])); }
;     const float u = pmax - PSH;
;     if (__builtin_expect(!first && __all(u <= THR2), 1)) { alpha = 1.f; }
;     else { const float dl = first ? u : fmaxf(u, 0.f); alpha = __builtin_amdgcn_exp2f(-dl); m_reg += dl;
; #pragma unroll
;         for (int r = 0; r < 16; ++r) { p0[r] -= dl; p1[r] -= dl; } }
; #pragma unroll
;     for (int r = 0; r < 16; ++r) p0[r] = __builtin_amdgcn_exp2f(p0[r]);
; }
; __device__ __forceinline__ void finishSM(f32x16& p0, f32x16& p1, float alpha, float& l_reg, v8i& pa) {
; #pragma unroll
;     for (int r = 0; r < 16; ++r) p1[r] = __builtin_amdgcn_exp2f(p1[r]);
;     float sa = p0[0] + p0[1], sb = p0[2] + p0[3], sc = p0[4] + p0[5], sd = p0[6] + p0[7];
;     sa += p0[8]; sb += p0[9]; sc += p0[10]; sd += p0[11]; sa += p0[12]; sb += p0[13]; sc += p0[14]; sd += p0[15];
; #pragma unroll
;     for (int r = 0; r < 16; r += 4) { sa += p1[r]; sb += p1[r + 1]; sc += p1[r + 2]; sd += p1[r + 3]; }
;     float ps = (sa + sb) + (sc + sd);
;     { auto rr = __builtin_amdgcn_permlane32_swap(__float_as_uint(ps), __float_as_uint(ps), false, false);
;       ps = __uint_as_float(rr[0]) + __uint_as_float(rr[1]); }
;     l_reg = l_reg * alpha + ps;
; #pragma unroll
;     for (int c = 0; c < 4; ++c) { pa[c] = (int)pk4_fp8(p0[4 * c], p0[4 * c + 1], p0[4 * c + 2], p0[4 * c + 3]);
;         pa[4 + c] = (int)pk4_fp8(p1[4 * c], p1[4 * c + 1], p1[4 * c + 2], p1[4 * c + 3]); }
; }
; __device__ __forceinline__ void qkt(f32x16& p0, f32x16& p1, const float m_reg, const char* Ks, const v8i* q8, int r32, int hi) {
;     { const float ini = PSH - m_reg;
.LBB0_563:
	v_sub_f32_e32 v64, 0x40400000, v180
	v_mov_b32_e32 v65, v64
	v_mov_b32_e32 v66, v64
	v_mov_b32_e32 v67, v64
	v_mov_b32_e32 v68, v64
	v_mov_b32_e32 v69, v64
	v_mov_b32_e32 v70, v64
	v_mov_b32_e32 v71, v64
	v_mov_b32_e32 v72, v64
	v_mov_b32_e32 v73, v64
	v_mov_b32_e32 v74, v64
	v_mov_b32_e32 v75, v64
	v_mov_b32_e32 v76, v64
	v_mov_b32_e32 v77, v64
	v_mov_b32_e32 v78, v64
	v_mov_b32_e32 v79, v64
	v_exp_f32_e32 v231, v80
	v_exp_f32_e32 v233, v81
	s_waitcnt lgkmcnt(0)
	v_mfma_scale_f32_32x32x64_f8f6f4 v[96:111], v[96:103], v[120:127], v[64:79], v201, v200 op_sel_hi:[0,0,0]
	v_exp_f32_e32 v225, v82
	v_exp_f32_e32 v226, v83
	v_exp_f32_e32 v232, v84
	v_exp_f32_e32 v234, v85
	v_exp_f32_e32 v229, v86
	v_exp_f32_e32 v230, v87
	v_add_f32_e32 v80, v216, v215
	v_add_f32_e32 v81, v194, v192
	v_add_f32_e32 v82, v214, v213
	v_add_f32_e32 v83, v212, v211
	v_exp_f32_e32 v227, v88
	v_exp_f32_e32 v228, v89
	v_exp_f32_e32 v219, v90
	v_exp_f32_e32 v220, v91
	v_add_f32_e32 v80, v193, v80
	v_mfma_scale_f32_32x32x64_f8f6f4 v[64:79], v[136:143], v[120:127], v[64:79], v201, v200 op_sel_hi:[0,0,0]
	ds_read_b128 v[136:139], v164 offset:64
	ds_read_b128 v[140:143], v164 offset:80
	ds_read_b128 v[144:147], v164 offset:6720
	ds_read_b128 v[148:151], v164 offset:6736
	v_add_f32_e32 v81, v195, v81
	v_add_f32_e32 v82, v186, v82
	v_add_f32_e32 v83, v187, v83
	v_exp_f32_e32 v223, v92
	v_exp_f32_e32 v224, v93
	v_exp_f32_e32 v221, v94
	v_exp_f32_e32 v222, v95
	v_add_f32_e32 v80, v190, v80
	v_add_f32_e32 v81, v191, v81
	v_add_f32_e32 v82, v188, v82
	v_add_f32_e32 v83, v189, v83
	v_add_f32_e32 v80, v80, v231
	v_add_f32_e32 v81, v81, v233
	v_add_f32_e32 v82, v82, v225
	s_waitcnt lgkmcnt(0)
	v_mfma_scale_f32_32x32x64_f8f6f4 v[96:111], v[136:143], v[128:135], v[96:111], v201, v200 op_sel_hi:[0,0,0]
	v_add_f32_e32 v83, v83, v226
	v_add_f32_e32 v80, v232, v80
	v_add_f32_e32 v81, v234, v81
	v_add_f32_e32 v82, v229, v82
	v_add_f32_e32 v83, v230, v83
	v_add_f32_e32 v80, v227, v80
	v_add_f32_e32 v81, v228, v81
	v_add_f32_e32 v82, v219, v82
	v_add_f32_e32 v83, v220, v83
	v_add_f32_e32 v80, v223, v80
	v_add_f32_e32 v81, v224, v81
	v_add_f32_e32 v82, v221, v82
	v_add_f32_e32 v83, v222, v83
	v_add_f32_e32 v80, v81, v80
	v_add_f32_e32 v81, v82, v83
	v_mfma_scale_f32_32x32x64_f8f6f4 v[64:79], v[144:151], v[128:135], v[64:79], v201, v200 op_sel_hi:[0,0,0]
	ds_read_b128 v[136:139], v164 offset:128
	ds_read_b128 v[140:143], v164 offset:144
	ds_read_b128 v[144:147], v164 offset:6784
	ds_read_b128 v[148:151], v164 offset:6800
	v_add_f32_e32 v217, v81, v80
	v_mov_b32_e32 v218, v217
	v_cvt_pk_fp8_f32 v236, v215, v216
	v_cvt_pk_fp8_f32 v240, v231, v233
	v_cvt_pk_fp8_f32 v237, v213, v214
	v_cvt_pk_fp8_f32 v241, v232, v234
	v_cvt_pk_fp8_f32 v238, v193, v195
	v_cvt_pk_fp8_f32 v242, v227, v228
	v_cvt_pk_fp8_f32 v239, v190, v191
	v_cvt_pk_fp8_f32 v243, v223, v224
	v_permlane32_swap_b32_e32 v217, v218
	s_waitcnt lgkmcnt(0)
	v_mfma_scale_f32_32x32x64_f8f6f4 v[96:111], v[136:143], v[112:119], v[96:111], v201, v200 op_sel_hi:[0,0,0]
	v_cvt_pk_fp8_f32 v236, v192, v194 op_sel:[0,0,1]
	v_cvt_pk_fp8_f32 v240, v225, v226 op_sel:[0,0,1]
	v_cvt_pk_fp8_f32 v237, v211, v212 op_sel:[0,0,1]
	v_cvt_pk_fp8_f32 v241, v229, v230 op_sel:[0,0,1]
	v_cvt_pk_fp8_f32 v238, v186, v187 op_sel:[0,0,1]
	v_cvt_pk_fp8_f32 v242, v219, v220 op_sel:[0,0,1]
	v_cvt_pk_fp8_f32 v239, v188, v189 op_sel:[0,0,1]
	v_cvt_pk_fp8_f32 v243, v221, v222 op_sel:[0,0,1]
	v_mfma_scale_f32_32x32x64_f8f6f4 v[64:79], v[144:151], v[112:119], v[64:79], v201, v200 op_sel_hi:[0,0,0]
	v_add3_u32 v84, s12, v161, v179
	ds_read_b128 v[144:147], v84 offset:13312
	ds_read_b128 v[148:151], v84 offset:13328
	ds_read_b128 v[136:139], v84 offset:15872
	ds_read_b128 v[140:143], v84 offset:15888
	ds_read_b128 v[88:91], v84 offset:18432
	ds_read_b128 v[92:95], v84 offset:18448
	ds_read_b128 v[80:83], v84 offset:20992
	ds_read_b128 v[84:87], v84 offset:21008
	s_nop 2
	v_max_f32_e32 v164, v96, v97
	v_max3_f32 v165, v99, v100, v101
	v_max3_f32 v164, v164, v98, v108
	v_max3_f32 v165, v165, v110, v111
	v_max3_f32 v166, v102, v103, v104
	v_max3_f32 v167, v105, v106, v107
	s_waitcnt lgkmcnt(0)
	v_mfma_scale_f32_32x32x64_f8f6f4 v[0:15], v[236:243], v[144:151], v[0:15], v201, v201 op_sel_hi:[0,0,0]
	v_max3_f32 v164, v164, v109, v68
	v_max3_f32 v165, v165, v70, v71
	v_max3_f32 v166, v166, v64, v65
	v_max3_f32 v167, v167, v66, v67
	v_max3_f32 v164, v164, v69, v76
	v_max3_f32 v165, v165, v78, v79
	v_max3_f32 v166, v166, v72, v73
	v_max3_f32 v167, v167, v74, v75
	v_mfma_scale_f32_32x32x64_f8f6f4 v[48:63], v[236:243], v[136:143], v[48:63], v201, v201 op_sel_hi:[0,0,0]
	v_max3_f32 v164, v164, v77, v165
	v_max3_f32 v164, v164, v166, v167
	v_mov_b32_e32 v165, v164
	s_nop 1
	v_permlane32_swap_b32_e32 v164, v165
	v_max_f32_e32 v164, v164, v165
	v_add_f32_e32 v165, 0xc0400000, v164
	s_mov_b32 s0, 0x40b8aa3b
	v_cmp_ge_f32_e32 vcc, s0, v165
	s_cmp_eq_u64 vcc, exec
	v_mov_b32_e32 v184, 1.0
	s_cbranch_scc0 .LBB0_571
